# row phases: cross-row hops of the wave reduction via v_permlane16/32_swap instead of ds_bpermute round trips (14 hops)
# speedup vs baseline: 1.0061x; 1.0061x over previous
.LBB0_175:
	global_load_dwordx2 v[30:31], v[22:23], off offset:1536
	global_load_dwordx2 v[28:29], v[22:23], off
	global_load_dwordx2 v[26:27], v[22:23], off offset:512
	global_load_dwordx2 v[24:25], v[22:23], off offset:1024
	s_add_i32 s4, s6, 0xfffffc00
	s_lshr_b32 s4, s4, 12
	s_mulk_i32 s4, 0x1800
	s_cmpk_gt_i32 s6, 0x3ff
	s_cselect_b32 s12, s4, 0x6000
	s_lshl_b64 s[4:5], s[12:13], 2
	v_lshl_add_u64 v[72:73], v[20:21], 0, s[4:5]
	v_lshl_add_u64 v[70:71], v[18:19], 0, s[4:5]
	global_load_dwordx4 v[36:39], v[72:73], off
	global_load_dwordx4 v[40:43], v[72:73], off offset:1024
	global_load_dwordx4 v[44:47], v[72:73], off offset:2048
	global_load_dwordx4 v[48:51], v[72:73], off offset:3072
	global_load_dwordx4 v[52:55], v[70:71], off
	global_load_dwordx4 v[56:59], v[70:71], off offset:1024
	global_load_dwordx4 v[60:63], v[70:71], off offset:2048
	global_load_dwordx4 v[64:67], v[70:71], off offset:3072
	v_add_co_u32_e32 v68, vcc, s14, v22
	s_add_i32 s6, s6, s8
	s_nop 0
	v_addc_co_u32_e32 v69, vcc, 0, v23, vcc
	v_lshl_add_u64 v[22:23], v[22:23], 0, s[10:11]
	s_cmpk_lt_i32 s6, 0x4400
	s_waitcnt vmcnt(11)
	v_lshlrev_b32_e32 v71, 16, v30
	s_waitcnt vmcnt(10)
	v_lshlrev_b32_e32 v74, 16, v28
	v_and_b32_e32 v75, 0xffff0000, v28
	v_lshlrev_b32_e32 v28, 16, v29
	v_and_b32_e32 v29, 0xffff0000, v29
	s_waitcnt vmcnt(9)
	v_lshlrev_b32_e32 v77, 16, v27
	v_lshlrev_b32_e32 v76, 16, v26
	v_and_b32_e32 v27, 0xffff0000, v27
	v_and_b32_e32 v26, 0xffff0000, v26
	v_mul_f32_e32 v70, v29, v29
	v_mul_f32_e32 v82, v75, v75
	v_mov_b32_e32 v83, v71
	s_waitcnt vmcnt(8)
	v_lshlrev_b32_e32 v78, 16, v24
	v_and_b32_e32 v79, 0xffff0000, v24
	v_lshlrev_b32_e32 v24, 16, v25
	v_and_b32_e32 v25, 0xffff0000, v25
	v_pk_mul_f32 v[80:81], v[26:27], v[26:27]
	v_pk_fma_f32 v[90:91], v[28:29], v[28:29], v[70:71] op_sel_hi:[1,1,0]
	v_pk_fma_f32 v[92:93], v[74:75], v[74:75], v[82:83] op_sel_hi:[1,1,0]
	v_and_b32_e32 v73, 0xffff0000, v30
	v_lshlrev_b32_e32 v30, 16, v31
	v_and_b32_e32 v31, 0xffff0000, v31
	v_mul_f32_e32 v84, v79, v79
	v_mul_f32_e32 v86, v25, v25
	v_pk_fma_f32 v[80:81], v[76:77], v[76:77], v[80:81]
	v_mov_b32_e32 v70, v92
	v_mov_b32_e32 v82, v90
	v_mul_f32_e32 v35, v73, v73
	v_mul_f32_e32 v94, v30, v30
	v_mul_f32_e32 v95, v31, v31
	v_mov_b32_e32 v88, v77
	v_mov_b32_e32 v89, v27
	v_mov_b32_e32 v72, v71
	v_pk_fma_f32 v[84:85], v[78:79], v[78:79], v[84:85] op_sel_hi:[1,1,0]
	v_pk_fma_f32 v[86:87], v[24:25], v[24:25], v[86:87] op_sel_hi:[1,1,0]
	v_mov_b32_e32 v77, v26
	v_pk_add_f32 v[26:27], v[92:93], v[90:91]
	v_pk_add_f32 v[80:81], v[80:81], v[80:81] op_sel:[0,1] op_sel_hi:[1,0]
	v_pk_mul_f32 v[70:71], v[70:71], v[82:83]
	v_mov_b32_e32 v85, v94
	v_mov_b32_e32 v87, v95
	v_mov_b32_e32 v81, v35
	v_mov_b32_e32 v27, v71
	v_pk_add_f32 v[82:83], v[84:85], v[86:87]
	v_pk_add_f32 v[26:27], v[26:27], v[80:81]
	s_waitcnt vmcnt(7)
	v_pk_add_f32 v[38:39], v[38:39], 1.0 op_sel_hi:[1,0]
	v_pk_add_f32 v[26:27], v[26:27], v[82:83]
	v_pk_add_f32 v[36:37], v[36:37], 1.0 op_sel_hi:[1,0]
	v_add_f32_e32 v26, v26, v27
	s_waitcnt vmcnt(6)
	v_pk_add_f32 v[42:43], v[42:43], 1.0 op_sel_hi:[1,0]
	v_pk_add_f32 v[40:41], v[40:41], 1.0 op_sel_hi:[1,0]
	v_add_f32_dpp v26, v26, v26 row_ror:8 row_mask:0xf bank_mask:0xf bound_ctrl:1
	s_waitcnt vmcnt(5)
	v_pk_add_f32 v[46:47], v[46:47], 1.0 op_sel_hi:[1,0]
	v_pk_add_f32 v[44:45], v[44:45], 1.0 op_sel_hi:[1,0]
	v_add_f32_dpp v26, v26, v26 row_ror:4 row_mask:0xf bank_mask:0xf bound_ctrl:1
	s_waitcnt vmcnt(4)
	v_pk_add_f32 v[50:51], v[50:51], 1.0 op_sel_hi:[1,0]
	v_pk_add_f32 v[48:49], v[48:49], 1.0 op_sel_hi:[1,0]
	v_add_f32_dpp v26, v26, v26 row_ror:2 row_mask:0xf bank_mask:0xf bound_ctrl:1
	s_nop 1
	v_add_f32_dpp v26, v26, v26 row_ror:1 row_mask:0xf bank_mask:0xf bound_ctrl:1
	v_mov_b32_e32 v27, v26
	s_nop 1
	v_permlane16_swap_b32_e32 v26, v27
	s_waitcnt lgkmcnt(0)
	v_add_f32_e32 v26, v26, v27
	v_mov_b32_e32 v27, v26
	s_nop 1
	v_permlane32_swap_b32_e32 v26, v27
	s_waitcnt lgkmcnt(0)
	v_add_f32_e32 v26, v26, v27
	v_fmamk_f32 v26, v26, 0x3a800000, v33
	v_mul_f32_e32 v27, 0x4f800000, v26
	v_cmp_gt_f32_e32 vcc, s7, v26
	s_nop 1
	v_cndmask_b32_e32 v26, v26, v27, vcc
	v_sqrt_f32_e32 v27, v26
	s_nop 0
	v_add_u32_e32 v35, -1, v27
	v_add_u32_e32 v70, 1, v27
	v_fma_f32 v71, -v35, v27, v26
	v_fma_f32 v80, -v70, v27, v26
	v_cmp_ge_f32_e64 s[4:5], 0, v71
	s_nop 1
	v_cndmask_b32_e64 v27, v27, v35, s[4:5]
	v_cmp_lt_f32_e64 s[4:5], 0, v80
	s_nop 1
	v_cndmask_b32_e64 v27, v27, v70, s[4:5]
	v_mul_f32_e32 v35, 0x37800000, v27
	v_cndmask_b32_e32 v27, v27, v35, vcc
	v_cmp_class_f32_e32 vcc, v26, v34
	s_nop 1
	v_cndmask_b32_e32 v26, v27, v26, vcc
	v_div_scale_f32 v27, s[4:5], v26, v26, 1.0
	v_rcp_f32_e32 v70, v27
	v_div_scale_f32 v35, vcc, 1.0, v26, 1.0
	v_fma_f32 v71, -v27, v70, 1.0
	v_fmac_f32_e32 v70, v71, v70
	v_mul_f32_e32 v71, v35, v70
	v_fma_f32 v80, -v27, v71, v35
	v_fmac_f32_e32 v71, v80, v70
	v_fma_f32 v27, -v27, v71, v35
	v_div_fmas_f32 v27, v27, v70, v71
	v_div_fixup_f32 v26, v27, v26, 1.0
	v_pk_mul_f32 v[28:29], v[28:29], v[26:27] op_sel_hi:[1,0]
	v_pk_mul_f32 v[70:71], v[74:75], v[26:27] op_sel_hi:[1,0]
	v_pk_mul_f32 v[74:75], v[88:89], v[26:27] op_sel_hi:[1,0]
	v_pk_mul_f32 v[76:77], v[76:77], v[26:27] op_sel_hi:[1,0]
	v_pk_mul_f32 v[24:25], v[24:25], v[26:27] op_sel_hi:[1,0]
	v_pk_mul_f32 v[78:79], v[78:79], v[26:27] op_sel_hi:[1,0]
	v_pk_mul_f32 v[72:73], v[72:73], v[26:27] op_sel_hi:[1,0]
	v_pk_mul_f32 v[26:27], v[30:31], v[26:27] op_sel_hi:[1,0]
	v_pk_mul_f32 v[30:31], v[2:3], v[70:71]
	v_pk_mul_f32 v[28:29], v[4:5], v[28:29]
	v_pk_mul_f32 v[70:71], v[6:7], v[76:77]
	v_pk_mul_f32 v[74:75], v[8:9], v[74:75]
	v_pk_mul_f32 v[76:77], v[10:11], v[78:79]
	v_pk_mul_f32 v[24:25], v[12:13], v[24:25]
	v_pk_mul_f32 v[26:27], v[16:17], v[26:27]
	v_pk_mul_f32 v[72:73], v[14:15], v[72:73]
	s_waitcnt vmcnt(3)
	v_pk_fma_f32 v[28:29], v[38:39], v[28:29], v[54:55]
	v_pk_fma_f32 v[30:31], v[36:37], v[30:31], v[52:53]
	s_waitcnt vmcnt(2)
	v_pk_fma_f32 v[36:37], v[42:43], v[74:75], v[58:59]
	v_pk_fma_f32 v[38:39], v[40:41], v[70:71], v[56:57]
	s_waitcnt vmcnt(1)
	v_pk_fma_f32 v[24:25], v[46:47], v[24:25], v[62:63]
	v_pk_fma_f32 v[40:41], v[44:45], v[76:77], v[60:61]
	s_waitcnt vmcnt(0)
	v_pk_fma_f32 v[42:43], v[48:49], v[72:73], v[64:65]
	v_pk_fma_f32 v[26:27], v[50:51], v[26:27], v[66:67]
	v_bfe_u32 v35, v30, 16, 1
	v_bfe_u32 v45, v28, 16, 1
	v_bfe_u32 v44, v31, 16, 1
	v_bfe_u32 v46, v29, 16, 1
	v_bfe_u32 v47, v38, 16, 1
	v_bfe_u32 v48, v39, 16, 1
	v_bfe_u32 v49, v36, 16, 1
	v_bfe_u32 v51, v40, 16, 1
	v_bfe_u32 v52, v41, 16, 1
	v_bfe_u32 v53, v24, 16, 1
	v_bfe_u32 v54, v25, 16, 1
	v_bfe_u32 v55, v42, 16, 1
	v_bfe_u32 v56, v43, 16, 1
	v_bfe_u32 v57, v26, 16, 1
	v_bfe_u32 v58, v27, 16, 1
	v_add3_u32 v30, v30, v35, s9
	v_add3_u32 v28, v28, v45, s9
	v_bfe_u32 v50, v37, 16, 1
	v_add3_u32 v31, v31, v44, s9
	v_add3_u32 v29, v29, v46, s9
	v_add3_u32 v35, v38, v47, s9
	v_add3_u32 v38, v39, v48, s9
	v_add3_u32 v36, v36, v49, s9
	v_add3_u32 v39, v40, v51, s9
	v_add3_u32 v40, v41, v52, s9
	v_add3_u32 v24, v24, v53, s9
	v_add3_u32 v41, v25, v54, s9
	v_add3_u32 v25, v42, v55, s9
	v_add3_u32 v42, v43, v56, s9
	v_add3_u32 v26, v26, v57, s9
	v_add3_u32 v43, v27, v58, s9
	v_lshrrev_b32_e32 v27, 16, v30
	v_lshrrev_b32_e32 v28, 16, v28
	v_add3_u32 v37, v37, v50, s9
	v_lshrrev_b32_e32 v30, 16, v35
	v_lshrrev_b32_e32 v35, 16, v36
	v_lshrrev_b32_e32 v36, 16, v39
	v_lshrrev_b32_e32 v39, 16, v24
	v_lshrrev_b32_e32 v44, 16, v25
	v_lshrrev_b32_e32 v45, 16, v26
	v_and_or_b32 v24, v31, s3, v27
	v_and_or_b32 v25, v29, s3, v28
	v_and_or_b32 v26, v38, s3, v30
	v_and_or_b32 v27, v37, s3, v35
	v_and_or_b32 v28, v40, s3, v36
	v_and_or_b32 v29, v41, s3, v39
	v_and_or_b32 v30, v42, s3, v44
	v_and_or_b32 v31, v43, s3, v45
	global_store_dwordx2 v[68:69], v[24:25], off
	global_store_dwordx2 v[68:69], v[26:27], off offset:512
	global_store_dwordx2 v[68:69], v[28:29], off offset:1024
	global_store_dwordx2 v[68:69], v[30:31], off offset:1536
	s_cbranch_scc1 .LBB0_175

.LBB0_676:
	s_add_i32 s10, s6, 0xfffffc00
	s_lshr_b32 s10, s10, 12
	s_mulk_i32 s10, 0x1800
	s_and_b64 s[4:5], s[4:5], exec
	s_cselect_b32 s10, 0x6000, s10
	s_lshl_b64 s[4:5], s[10:11], 2
	v_pk_mul_f32 v[62:63], v[32:33], v[32:33]
	v_pk_mul_f32 v[64:65], v[30:31], v[30:31]
	v_lshl_add_u64 v[66:67], v[24:25], 0, s[4:5]
	v_pk_mul_f32 v[58:59], v[34:35], v[34:35]
	v_pk_mul_f32 v[60:61], v[44:45], v[44:45]
	global_load_dwordx4 v[18:21], v[66:67], off
	global_load_dwordx4 v[46:49], v[66:67], off offset:1024
	global_load_dwordx4 v[50:53], v[66:67], off offset:2048
	global_load_dwordx4 v[54:57], v[66:67], off offset:3072
	v_pk_mov_b32 v[66:67], v[64:65], v[62:63] op_sel:[1,0]
	v_mov_b32_e32 v65, v63
	v_pk_add_f32 v[62:63], v[66:67], v[64:65]
	v_pk_mov_b32 v[64:65], v[60:61], v[58:59] op_sel:[1,0]
	v_mov_b32_e32 v61, v59
	v_pk_add_f32 v[58:59], v[64:65], v[60:61]
	v_pk_add_f32 v[62:63], v[62:63], v[62:63] op_sel_hi:[0,1]
	v_pk_add_f32 v[58:59], v[58:59], v[58:59] op_sel_hi:[0,1]
	v_mul_f32_e32 v58, v42, v42
	v_pk_fma_f32 v[60:61], v[42:43], v[42:43], v[58:59] op_sel_hi:[1,1,0]
	v_mul_f32_e32 v58, v36, v36
	v_pk_fma_f32 v[64:65], v[36:37], v[36:37], v[58:59] op_sel_hi:[1,1,0]
	v_mul_f32_e32 v60, v38, v38
	v_mul_f32_e32 v64, v39, v39
	v_mul_f32_e32 v62, v40, v40
	v_mul_f32_e32 v58, v41, v41
	v_pk_add_f32 v[66:67], v[60:61], v[64:65]
	v_pk_add_f32 v[68:69], v[62:63], v[58:59]
	v_lshl_add_u64 v[74:75], v[22:23], 0, s[4:5]
	v_pk_add_f32 v[66:67], v[66:67], v[68:69]
	global_load_dwordx4 v[58:61], v[74:75], off offset:2048
	global_load_dwordx4 v[62:65], v[74:75], off offset:3072
	v_add_f32_e32 v76, v66, v67
	global_load_dwordx4 v[66:69], v[74:75], off
	global_load_dwordx4 v[70:73], v[74:75], off offset:1024
	v_add_f32_dpp v74, v76, v76 row_ror:8 row_mask:0xf bank_mask:0xf bound_ctrl:1
	s_add_i32 s6, s6, s8
	s_cmpk_lt_i32 s6, 0x4400
	v_add_f32_dpp v74, v74, v74 row_ror:4 row_mask:0xf bank_mask:0xf bound_ctrl:1
	s_waitcnt vmcnt(7)
	v_pk_add_f32 v[18:19], v[18:19], 1.0 op_sel_hi:[1,0]
	v_add_f32_dpp v74, v74, v74 row_ror:2 row_mask:0xf bank_mask:0xf bound_ctrl:1
	v_pk_add_f32 v[20:21], v[20:21], 1.0 op_sel_hi:[1,0]
	s_waitcnt vmcnt(6)
	v_pk_add_f32 v[46:47], v[46:47], 1.0 op_sel_hi:[1,0]
	v_add_f32_dpp v74, v74, v74 row_ror:1 row_mask:0xf bank_mask:0xf bound_ctrl:1
	v_mov_b32_e32 v75, v74
	s_nop 1
	v_permlane16_swap_b32_e32 v74, v75
	v_pk_add_f32 v[48:49], v[48:49], 1.0 op_sel_hi:[1,0]
	s_waitcnt vmcnt(5)
	v_pk_add_f32 v[50:51], v[50:51], 1.0 op_sel_hi:[1,0]
	v_pk_add_f32 v[52:53], v[52:53], 1.0 op_sel_hi:[1,0]
	s_waitcnt vmcnt(4)
	v_pk_add_f32 v[54:55], v[54:55], 1.0 op_sel_hi:[1,0]
	s_waitcnt lgkmcnt(0)
	v_add_f32_e32 v74, v74, v75
	v_mov_b32_e32 v75, v74
	s_nop 1
	v_permlane32_swap_b32_e32 v74, v75
	v_pk_add_f32 v[56:57], v[56:57], 1.0 op_sel_hi:[1,0]
	s_waitcnt lgkmcnt(0)
	v_add_f32_e32 v74, v74, v75
	v_fmamk_f32 v74, v74, 0x3a800000, v93
	v_mul_f32_e32 v75, 0x4f800000, v74
	v_cmp_gt_f32_e32 vcc, s35, v74
	s_nop 1
	v_cndmask_b32_e32 v74, v74, v75, vcc
	v_sqrt_f32_e32 v75, v74
	s_nop 0
	v_add_u32_e32 v76, -1, v75
	v_add_u32_e32 v77, 1, v75
	v_fma_f32 v78, -v76, v75, v74
	v_fma_f32 v79, -v77, v75, v74
	v_cmp_ge_f32_e64 s[4:5], 0, v78
	s_nop 1
	v_cndmask_b32_e64 v75, v75, v76, s[4:5]
	v_cmp_lt_f32_e64 s[4:5], 0, v79
	s_nop 1
	v_cndmask_b32_e64 v75, v75, v77, s[4:5]
	v_mul_f32_e32 v76, 0x37800000, v75
	v_cndmask_b32_e32 v75, v75, v76, vcc
	v_cmp_class_f32_e32 vcc, v74, v94
	s_nop 1
	v_cndmask_b32_e32 v74, v75, v74, vcc
	v_div_scale_f32 v75, s[4:5], v74, v74, 1.0
	v_rcp_f32_e32 v76, v75
	v_div_scale_f32 v77, vcc, 1.0, v74, 1.0
	v_fma_f32 v78, -v75, v76, 1.0
	v_fmac_f32_e32 v76, v78, v76
	v_mul_f32_e32 v78, v77, v76
	v_fma_f32 v79, -v75, v78, v77
	v_fmac_f32_e32 v78, v79, v76
	v_fma_f32 v75, -v75, v78, v77
	v_div_fmas_f32 v75, v75, v76, v78
	v_div_fixup_f32 v74, v75, v74, 1.0
	v_pk_mul_f32 v[30:31], v[30:31], v[74:75] op_sel_hi:[1,0]
	v_pk_mul_f32 v[32:33], v[32:33], v[74:75] op_sel_hi:[1,0]
	v_pk_mul_f32 v[30:31], v[2:3], v[30:31]
	v_pk_mul_f32 v[32:33], v[4:5], v[32:33]
	s_waitcnt vmcnt(1)
	v_pk_fma_f32 v[18:19], v[18:19], v[30:31], v[66:67]
	v_pk_fma_f32 v[20:21], v[20:21], v[32:33], v[68:69]
	v_bfe_u32 v30, v18, 16, 1
	v_add3_u32 v18, v18, v30, s33
	v_bfe_u32 v30, v19, 16, 1
	v_lshrrev_b32_e32 v18, 16, v18
	v_add3_u32 v19, v19, v30, s33
	v_and_or_b32 v18, v19, s3, v18
	v_bfe_u32 v19, v20, 16, 1
	v_add3_u32 v19, v20, v19, s33
	v_bfe_u32 v20, v21, 16, 1
	v_pk_mul_f32 v[44:45], v[44:45], v[74:75] op_sel_hi:[1,0]
	v_lshrrev_b32_e32 v19, 16, v19
	v_add3_u32 v20, v21, v20, s33
	v_pk_mul_f32 v[44:45], v[6:7], v[44:45]
	v_and_or_b32 v19, v20, s3, v19
	v_add_co_u32_e32 v20, vcc, s36, v28
	s_waitcnt vmcnt(0)
	v_pk_fma_f32 v[44:45], v[46:47], v[44:45], v[70:71]
	v_addc_co_u32_e32 v21, vcc, -1, v29, vcc
	v_pk_mul_f32 v[34:35], v[34:35], v[74:75] op_sel_hi:[1,0]
	global_store_dwordx2 v[20:21], v[18:19], off offset:-1536
	v_pk_mul_f32 v[34:35], v[8:9], v[34:35]
	v_pk_fma_f32 v[34:35], v[48:49], v[34:35], v[72:73]
	v_cvt_pk_bf16_f32 v18, v44, v45
	v_pk_mul_f32 v[42:43], v[42:43], v[74:75] op_sel_hi:[1,0]
	v_pk_mul_f32 v[42:43], v[10:11], v[42:43]
	v_pk_fma_f32 v[42:43], v[50:51], v[42:43], v[58:59]
	v_cvt_pk_bf16_f32 v19, v34, v35
	v_pk_mul_f32 v[36:37], v[36:37], v[74:75] op_sel_hi:[1,0]
	global_store_dwordx2 v[20:21], v[18:19], off offset:-1024
	v_pk_mul_f32 v[36:37], v[12:13], v[36:37]
	v_pk_fma_f32 v[36:37], v[52:53], v[36:37], v[60:61]
	v_cvt_pk_bf16_f32 v18, v42, v43
	v_pk_mul_f32 v[38:39], v[38:39], v[74:75] op_sel_hi:[1,0]
	v_pk_mul_f32 v[38:39], v[14:15], v[38:39]
	v_pk_fma_f32 v[38:39], v[54:55], v[38:39], v[62:63]
	v_cvt_pk_bf16_f32 v19, v36, v37
	v_pk_mul_f32 v[40:41], v[40:41], v[74:75] op_sel_hi:[1,0]
	global_store_dwordx2 v[20:21], v[18:19], off offset:-512
	v_pk_mul_f32 v[40:41], v[16:17], v[40:41]
	v_pk_fma_f32 v[40:41], v[56:57], v[40:41], v[64:65]
	v_cvt_pk_bf16_f32 v18, v38, v39
	v_cvt_pk_bf16_f32 v19, v40, v41
	v_lshl_add_u64 v[28:29], v[28:29], 0, s[12:13]
	global_store_dwordx2 v[20:21], v[18:19], off
	s_cbranch_scc0 .LBB0_679

.LBB0_891:
	v_pk_mul_f32 v[62:63], v[32:33], v[32:33]
	v_pk_mul_f32 v[64:65], v[30:31], v[30:31]
	v_pk_mul_f32 v[58:59], v[34:35], v[34:35]
	v_pk_mul_f32 v[60:61], v[38:39], v[38:39]
	v_pk_mov_b32 v[66:67], v[64:65], v[62:63] op_sel:[1,0]
	v_mov_b32_e32 v65, v63
	v_pk_add_f32 v[62:63], v[66:67], v[64:65]
	v_pk_mov_b32 v[64:65], v[60:61], v[58:59] op_sel:[1,0]
	v_mov_b32_e32 v61, v59
	v_pk_add_f32 v[58:59], v[64:65], v[60:61]
	s_add_i32 s10, s6, 0xfffffc00
	v_pk_add_f32 v[58:59], v[58:59], v[58:59] op_sel_hi:[0,1]
	v_mul_f32_e32 v58, v44, v44
	s_lshr_b32 s10, s10, 12
	v_pk_fma_f32 v[60:61], v[44:45], v[44:45], v[58:59] op_sel_hi:[1,1,0]
	v_mul_f32_e32 v58, v40, v40
	s_mulk_i32 s10, 0x1800
	s_and_b64 s[4:5], s[4:5], exec
	v_pk_add_f32 v[62:63], v[62:63], v[62:63] op_sel_hi:[0,1]
	v_pk_fma_f32 v[64:65], v[40:41], v[40:41], v[58:59] op_sel_hi:[1,1,0]
	s_cselect_b32 s10, 0x6000, s10
	v_mul_f32_e32 v60, v36, v36
	v_mul_f32_e32 v64, v37, v37
	v_mul_f32_e32 v62, v42, v42
	v_mul_f32_e32 v58, v43, v43
	s_lshl_b64 s[4:5], s[10:11], 2
	v_pk_add_f32 v[66:67], v[60:61], v[64:65]
	v_pk_add_f32 v[68:69], v[62:63], v[58:59]
	v_lshl_add_u64 v[54:55], v[24:25], 0, s[4:5]
	v_lshl_add_u64 v[70:71], v[22:23], 0, s[4:5]
	v_pk_add_f32 v[66:67], v[66:67], v[68:69]
	global_load_dwordx4 v[18:21], v[54:55], off
	global_load_dwordx4 v[46:49], v[54:55], off offset:1024
	global_load_dwordx4 v[50:53], v[54:55], off offset:2048
	s_nop 0
	global_load_dwordx4 v[54:57], v[54:55], off offset:3072
	s_nop 0
	global_load_dwordx4 v[58:61], v[70:71], off offset:2048
	global_load_dwordx4 v[62:65], v[70:71], off offset:3072
	v_add_f32_e32 v74, v66, v67
	global_load_dwordx4 v[66:69], v[70:71], off
	s_nop 0
	global_load_dwordx4 v[70:73], v[70:71], off offset:1024
	v_add_f32_dpp v74, v74, v74 row_ror:8 row_mask:0xf bank_mask:0xf bound_ctrl:1
	s_add_i32 s6, s6, s8
	s_cmpk_lt_i32 s6, 0x4400
	v_add_f32_dpp v74, v74, v74 row_ror:4 row_mask:0xf bank_mask:0xf bound_ctrl:1
	s_waitcnt vmcnt(7)
	v_pk_add_f32 v[18:19], v[18:19], 1.0 op_sel_hi:[1,0]
	v_add_f32_dpp v74, v74, v74 row_ror:2 row_mask:0xf bank_mask:0xf bound_ctrl:1
	v_pk_add_f32 v[20:21], v[20:21], 1.0 op_sel_hi:[1,0]
	s_waitcnt vmcnt(6)
	v_pk_add_f32 v[46:47], v[46:47], 1.0 op_sel_hi:[1,0]
	v_add_f32_dpp v74, v74, v74 row_ror:1 row_mask:0xf bank_mask:0xf bound_ctrl:1
	v_mov_b32_e32 v75, v74
	s_nop 1
	v_permlane16_swap_b32_e32 v74, v75
	v_pk_add_f32 v[48:49], v[48:49], 1.0 op_sel_hi:[1,0]
	s_waitcnt vmcnt(5)
	v_pk_add_f32 v[50:51], v[50:51], 1.0 op_sel_hi:[1,0]
	v_pk_add_f32 v[52:53], v[52:53], 1.0 op_sel_hi:[1,0]
	s_waitcnt vmcnt(4)
	v_pk_add_f32 v[54:55], v[54:55], 1.0 op_sel_hi:[1,0]
	s_waitcnt lgkmcnt(0)
	v_add_f32_e32 v74, v74, v75
	v_mov_b32_e32 v75, v74
	s_nop 1
	v_permlane32_swap_b32_e32 v74, v75
	v_pk_add_f32 v[56:57], v[56:57], 1.0 op_sel_hi:[1,0]
	s_waitcnt lgkmcnt(0)
	v_add_f32_e32 v74, v74, v75
	v_fmamk_f32 v74, v74, 0x3a800000, v95
	v_mul_f32_e32 v75, 0x4f800000, v74
	v_cmp_gt_f32_e32 vcc, s42, v74
	s_nop 1
	v_cndmask_b32_e32 v74, v74, v75, vcc
	v_sqrt_f32_e32 v75, v74
	s_nop 0
	v_add_u32_e32 v76, -1, v75
	v_add_u32_e32 v77, 1, v75
	v_fma_f32 v78, -v76, v75, v74
	v_fma_f32 v79, -v77, v75, v74
	v_cmp_ge_f32_e64 s[4:5], 0, v78
	s_nop 1
	v_cndmask_b32_e64 v75, v75, v76, s[4:5]
	v_cmp_lt_f32_e64 s[4:5], 0, v79
	s_nop 1
	v_cndmask_b32_e64 v75, v75, v77, s[4:5]
	v_mul_f32_e32 v76, 0x37800000, v75
	v_cndmask_b32_e32 v75, v75, v76, vcc
	v_cmp_class_f32_e32 vcc, v74, v96
	s_nop 1
	v_cndmask_b32_e32 v74, v75, v74, vcc
	v_div_scale_f32 v75, s[4:5], v74, v74, 1.0
	v_rcp_f32_e32 v76, v75
	v_div_scale_f32 v77, vcc, 1.0, v74, 1.0
	v_fma_f32 v78, -v75, v76, 1.0
	v_fmac_f32_e32 v76, v78, v76
	v_mul_f32_e32 v78, v77, v76
	v_fma_f32 v79, -v75, v78, v77
	v_fmac_f32_e32 v78, v79, v76
	v_fma_f32 v75, -v75, v78, v77
	v_div_fmas_f32 v75, v75, v76, v78
	v_div_fixup_f32 v74, v75, v74, 1.0
	v_pk_mul_f32 v[30:31], v[30:31], v[74:75] op_sel_hi:[1,0]
	v_pk_mul_f32 v[32:33], v[32:33], v[74:75] op_sel_hi:[1,0]
	v_pk_mul_f32 v[30:31], v[10:11], v[30:31]
	v_pk_mul_f32 v[32:33], v[12:13], v[32:33]
	s_waitcnt vmcnt(1)
	v_pk_fma_f32 v[18:19], v[18:19], v[30:31], v[66:67]
	v_pk_fma_f32 v[20:21], v[20:21], v[32:33], v[68:69]
	v_bfe_u32 v30, v18, 16, 1
	v_add3_u32 v18, v18, v30, s37
	v_bfe_u32 v30, v19, 16, 1
	v_lshrrev_b32_e32 v18, 16, v18
	v_add3_u32 v19, v19, v30, s37
	v_and_or_b32 v18, v19, s3, v18
	v_bfe_u32 v19, v20, 16, 1
	v_add3_u32 v19, v20, v19, s37
	v_bfe_u32 v20, v21, 16, 1
	v_pk_mul_f32 v[38:39], v[38:39], v[74:75] op_sel_hi:[1,0]
	v_lshrrev_b32_e32 v19, 16, v19
	v_add3_u32 v20, v21, v20, s37
	v_pk_mul_f32 v[38:39], v[2:3], v[38:39]
	v_and_or_b32 v19, v20, s3, v19
	v_add_co_u32_e32 v20, vcc, s43, v28
	s_waitcnt vmcnt(0)
	v_pk_fma_f32 v[38:39], v[46:47], v[38:39], v[70:71]
	v_addc_co_u32_e32 v21, vcc, -1, v29, vcc
	v_pk_mul_f32 v[34:35], v[34:35], v[74:75] op_sel_hi:[1,0]
	global_store_dwordx2 v[20:21], v[18:19], off offset:-1536
	v_pk_mul_f32 v[34:35], v[4:5], v[34:35]
	v_pk_fma_f32 v[34:35], v[48:49], v[34:35], v[72:73]
	v_cvt_pk_bf16_f32 v18, v38, v39
	v_pk_mul_f32 v[44:45], v[44:45], v[74:75] op_sel_hi:[1,0]
	v_pk_mul_f32 v[44:45], v[6:7], v[44:45]
	v_pk_fma_f32 v[44:45], v[50:51], v[44:45], v[58:59]
	v_cvt_pk_bf16_f32 v19, v34, v35
	v_pk_mul_f32 v[40:41], v[40:41], v[74:75] op_sel_hi:[1,0]
	global_store_dwordx2 v[20:21], v[18:19], off offset:-1024
	v_pk_mul_f32 v[40:41], v[8:9], v[40:41]
	v_pk_fma_f32 v[40:41], v[52:53], v[40:41], v[60:61]
	v_cvt_pk_bf16_f32 v18, v44, v45
	v_pk_mul_f32 v[36:37], v[36:37], v[74:75] op_sel_hi:[1,0]
	v_pk_mul_f32 v[36:37], v[14:15], v[36:37]
	v_pk_fma_f32 v[36:37], v[54:55], v[36:37], v[62:63]
	v_cvt_pk_bf16_f32 v19, v40, v41
	v_pk_mul_f32 v[42:43], v[42:43], v[74:75] op_sel_hi:[1,0]
	global_store_dwordx2 v[20:21], v[18:19], off offset:-512
	v_pk_mul_f32 v[42:43], v[16:17], v[42:43]
	v_pk_fma_f32 v[42:43], v[56:57], v[42:43], v[64:65]
	v_cvt_pk_bf16_f32 v18, v36, v37
	v_cvt_pk_bf16_f32 v19, v42, v43
	v_lshl_add_u64 v[28:29], v[28:29], 0, s[12:13]
	global_store_dwordx2 v[20:21], v[18:19], off
	s_cbranch_scc0 .LBB0_894

.LBB0_1683:
	v_and_b32_sdwa v52, v63, v74 dst_sel:DWORD dst_unused:UNUSED_PAD src0_sel:WORD_1 src1_sel:DWORD
	v_and_b32_sdwa v53, v62, v74 dst_sel:DWORD dst_unused:UNUSED_PAD src0_sel:WORD_1 src1_sel:DWORD
	v_add3_u32 v52, v63, v52, s21
	v_add3_u32 v53, v62, v53, s21
	v_and_b32_e32 v77, 0xffff0000, v52
	v_and_b32_e32 v76, 0xffff0000, v53
	v_and_b32_sdwa v52, v67, v74 dst_sel:DWORD dst_unused:UNUSED_PAD src0_sel:WORD_1 src1_sel:DWORD
	v_and_b32_sdwa v53, v66, v74 dst_sel:DWORD dst_unused:UNUSED_PAD src0_sel:WORD_1 src1_sel:DWORD
	v_add3_u32 v52, v67, v52, s21
	v_add3_u32 v53, v66, v53, s21
	v_and_b32_e32 v79, 0xffff0000, v52
	v_and_b32_e32 v78, 0xffff0000, v53
	v_and_b32_sdwa v52, v69, v74 dst_sel:DWORD dst_unused:UNUSED_PAD src0_sel:WORD_1 src1_sel:DWORD
	v_and_b32_sdwa v53, v68, v74 dst_sel:DWORD dst_unused:UNUSED_PAD src0_sel:WORD_1 src1_sel:DWORD
	v_add3_u32 v52, v69, v52, s21
	v_add3_u32 v53, v68, v53, s21
	v_and_b32_e32 v81, 0xffff0000, v52
	v_and_b32_e32 v80, 0xffff0000, v53
	v_mov_b32_e32 v52, v44
	v_mov_b32_e32 v53, v44
	v_pk_mul_f32 v[26:27], v[44:45], v[26:27]
	v_lshlrev_b32_e32 v50, 16, v46
	v_and_b32_e32 v51, 0xffff0000, v46
	v_pk_mul_f32 v[28:29], v[52:53], v[28:29]
	v_mov_b32_e32 v44, v42
	v_mov_b32_e32 v45, v42
	v_pk_fma_f32 v[22:23], v[42:43], v[22:23], v[26:27]
	v_lshlrev_b32_e32 v46, 16, v47
	v_and_b32_e32 v47, 0xffff0000, v47
	v_pk_fma_f32 v[24:25], v[44:45], v[24:25], v[28:29]
	s_waitcnt vmcnt(0)
	v_pk_fma_f32 v[18:19], v[18:19], v[22:23], v[50:51]
	v_pk_fma_f32 v[20:21], v[20:21], v[24:25], v[46:47]
	v_bfe_u32 v22, v18, 16, 1
	v_bfe_u32 v23, v19, 16, 1
	v_and_b32_sdwa v24, v19, v74 dst_sel:DWORD dst_unused:UNUSED_PAD src0_sel:WORD_1 src1_sel:DWORD
	v_and_b32_sdwa v25, v18, v74 dst_sel:DWORD dst_unused:UNUSED_PAD src0_sel:WORD_1 src1_sel:DWORD
	v_add3_u32 v22, v18, v22, s21
	v_add3_u32 v23, v19, v23, s21
	v_add3_u32 v19, v19, v24, s21
	v_add3_u32 v18, v18, v25, s21
	v_and_b32_e32 v47, 0xffff0000, v19
	v_and_b32_e32 v46, 0xffff0000, v18
	v_and_b32_sdwa v18, v21, v74 dst_sel:DWORD dst_unused:UNUSED_PAD src0_sel:WORD_1 src1_sel:DWORD
	v_and_b32_sdwa v19, v20, v74 dst_sel:DWORD dst_unused:UNUSED_PAD src0_sel:WORD_1 src1_sel:DWORD
	v_lshrrev_b32_e32 v22, 16, v22
	v_add3_u32 v18, v21, v18, s21
	v_add3_u32 v19, v20, v19, s21
	v_and_or_b32 v22, v23, s9, v22
	v_bfe_u32 v23, v20, 16, 1
	v_and_b32_e32 v83, 0xffff0000, v18
	v_and_b32_e32 v82, 0xffff0000, v19
	v_pk_mov_b32 v[18:19], v[76:77], v[48:49] op_sel:[1,0]
	v_add3_u32 v23, v20, v23, s21
	v_pk_mul_f32 v[18:19], v[18:19], v[18:19]
	v_mov_b32_e32 v20, v76
	v_mov_b32_e32 v21, v49
	v_or_b32_sdwa v23, v83, v23 dst_sel:DWORD dst_unused:UNUSED_PAD src0_sel:DWORD src1_sel:WORD_1
	v_pk_fma_f32 v[18:19], v[20:21], v[20:21], v[18:19]
	s_lshl_b64 s[4:5], s[10:11], 2
	global_store_dwordx2 v[40:41], v[22:23], off offset:1536
	v_pk_add_f32 v[50:51], v[18:19], v[18:19] op_sel:[0,1] op_sel_hi:[1,0]
	v_pk_mov_b32 v[18:19], v[78:79], v[64:65] op_sel:[1,0]
	v_lshl_add_u64 v[54:55], v[38:39], 0, s[4:5]
	v_pk_mul_f32 v[52:53], v[18:19], v[18:19]
	global_load_dwordx4 v[18:21], v[54:55], off
	global_load_dwordx4 v[22:25], v[54:55], off offset:1024
	global_load_dwordx4 v[26:29], v[54:55], off offset:2048
	global_load_dwordx4 v[42:45], v[54:55], off offset:3072
	v_mov_b32_e32 v54, v78
	v_mov_b32_e32 v55, v65
	v_pk_fma_f32 v[52:53], v[54:55], v[54:55], v[52:53]
	v_mul_f32_e32 v54, v81, v81
	v_mul_f32_e32 v56, v59, v59
	v_pk_add_f32 v[52:53], v[52:53], v[52:53] op_sel:[0,1] op_sel_hi:[1,0]
	v_pk_fma_f32 v[54:55], v[80:81], v[80:81], v[54:55] op_sel_hi:[1,1,0]
	v_pk_fma_f32 v[56:57], v[58:59], v[58:59], v[56:57] op_sel_hi:[1,1,0]
	v_pk_mul_f32 v[60:61], v[46:47], v[46:47]
	v_pk_mul_f32 v[62:63], v[82:83], v[82:83]
	v_mov_b32_e32 v51, v60
	v_mov_b32_e32 v53, v61
	v_mov_b32_e32 v55, v63
	v_mov_b32_e32 v57, v62
	v_pk_add_f32 v[50:51], v[50:51], v[52:53]
	v_pk_add_f32 v[52:53], v[54:55], v[56:57]
	v_lshl_add_u64 v[84:85], v[36:37], 0, s[4:5]
	v_pk_add_f32 v[50:51], v[50:51], v[52:53]
	s_add_i32 s8, s8, s12
	v_add_f32_e32 v60, v50, v51
	global_load_dwordx4 v[50:53], v[84:85], off offset:2048
	global_load_dwordx4 v[54:57], v[84:85], off offset:3072
	v_add_f32_dpp v60, v60, v60 row_ror:8 row_mask:0xf bank_mask:0xf bound_ctrl:1
	s_add_i32 s14, s14, s3
	s_cmpk_lt_i32 s8, 0x4400
	v_add_f32_dpp v75, v60, v60 row_ror:4 row_mask:0xf bank_mask:0xf bound_ctrl:1
	global_load_dwordx4 v[60:63], v[84:85], off
	global_load_dwordx4 v[66:69], v[84:85], off offset:1024
	v_add_f32_dpp v75, v75, v75 row_ror:2 row_mask:0xf bank_mask:0xf bound_ctrl:1
	s_waitcnt vmcnt(7)
	v_pk_add_f32 v[18:19], v[18:19], 1.0 op_sel_hi:[1,0]
	v_add_f32_dpp v75, v75, v75 row_ror:1 row_mask:0xf bank_mask:0xf bound_ctrl:1
	v_mov_b32_e32 v84, v75
	s_nop 1
	v_permlane16_swap_b32_e32 v75, v84
	s_waitcnt vmcnt(4)
	v_pk_add_f32 v[42:43], v[42:43], 1.0 op_sel_hi:[1,0]
	v_pk_add_f32 v[20:21], v[20:21], 1.0 op_sel_hi:[1,0]
	v_pk_add_f32 v[22:23], v[22:23], 1.0 op_sel_hi:[1,0]
	v_pk_add_f32 v[24:25], v[24:25], 1.0 op_sel_hi:[1,0]
	s_waitcnt lgkmcnt(0)
	v_add_f32_e32 v75, v75, v84
	v_mov_b32_e32 v84, v75
	s_nop 1
	v_permlane32_swap_b32_e32 v75, v84
	v_pk_add_f32 v[26:27], v[26:27], 1.0 op_sel_hi:[1,0]
	v_pk_add_f32 v[28:29], v[28:29], 1.0 op_sel_hi:[1,0]
	v_pk_add_f32 v[44:45], v[44:45], 1.0 op_sel_hi:[1,0]
	s_waitcnt lgkmcnt(0)
	v_add_f32_e32 v75, v75, v84
	v_fmamk_f32 v75, v75, 0x3a800000, v72
	v_mul_f32_e32 v84, 0x4f800000, v75
	v_cmp_gt_f32_e32 vcc, s22, v75
	s_nop 1
	v_cndmask_b32_e32 v75, v75, v84, vcc
	v_sqrt_f32_e32 v84, v75
	s_nop 0
	v_add_u32_e32 v85, -1, v84
	v_fma_f32 v86, -v85, v84, v75
	v_cmp_ge_f32_e64 s[4:5], 0, v86
	v_add_u32_e32 v86, 1, v84
	s_nop 0
	v_cndmask_b32_e64 v85, v84, v85, s[4:5]
	v_fma_f32 v84, -v86, v84, v75
	v_cmp_lt_f32_e64 s[4:5], 0, v84
	s_nop 1
	v_cndmask_b32_e64 v84, v85, v86, s[4:5]
	v_mul_f32_e32 v85, 0x37800000, v84
	v_cndmask_b32_e32 v84, v84, v85, vcc
	v_cmp_class_f32_e32 vcc, v75, v73
	s_nop 1
	v_cndmask_b32_e32 v75, v84, v75, vcc
	v_div_scale_f32 v84, s[4:5], v75, v75, 1.0
	v_rcp_f32_e32 v85, v84
	s_nop 0
	v_fma_f32 v86, -v84, v85, 1.0
	v_fmac_f32_e32 v85, v86, v85
	v_div_scale_f32 v86, vcc, 1.0, v75, 1.0
	v_mul_f32_e32 v87, v86, v85
	v_fma_f32 v88, -v84, v87, v86
	v_fmac_f32_e32 v87, v88, v85
	v_fma_f32 v84, -v84, v87, v86
	v_div_fmas_f32 v84, v84, v85, v87
	v_div_fixup_f32 v84, v84, v75, 1.0
	v_pk_mul_f32 v[76:77], v[76:77], v[84:85] op_sel_hi:[1,0]
	v_pk_mul_f32 v[46:47], v[46:47], v[84:85] op_sel_hi:[1,0]
	v_pk_mul_f32 v[76:77], v[10:11], v[76:77]
	v_pk_mul_f32 v[46:47], v[14:15], v[46:47]
	s_waitcnt vmcnt(1)
	v_pk_fma_f32 v[18:19], v[18:19], v[76:77], v[60:61]
	v_pk_mul_f32 v[48:49], v[48:49], v[84:85] op_sel_hi:[1,0]
	v_pk_fma_f32 v[42:43], v[42:43], v[46:47], v[54:55]
	v_bfe_u32 v46, v18, 16, 1
	v_pk_mul_f32 v[48:49], v[12:13], v[48:49]
	v_add3_u32 v18, v18, v46, s21
	v_bfe_u32 v46, v19, 16, 1
	v_pk_fma_f32 v[20:21], v[20:21], v[48:49], v[62:63]
	v_lshrrev_b32_e32 v18, 16, v18
	v_add3_u32 v19, v19, v46, s21
	v_and_or_b32 v18, v19, s9, v18
	v_bfe_u32 v19, v20, 16, 1
	v_add3_u32 v19, v20, v19, s21
	v_bfe_u32 v20, v21, 16, 1
	v_pk_mul_f32 v[78:79], v[78:79], v[84:85] op_sel_hi:[1,0]
	v_lshrrev_b32_e32 v19, 16, v19
	v_add3_u32 v20, v21, v20, s21
	v_pk_mul_f32 v[78:79], v[2:3], v[78:79]
	v_and_or_b32 v19, v20, s9, v19
	v_add_co_u32_e32 v20, vcc, s23, v40
	s_waitcnt vmcnt(0)
	v_pk_fma_f32 v[22:23], v[22:23], v[78:79], v[66:67]
	v_addc_co_u32_e32 v21, vcc, 0, v41, vcc
	v_pk_mul_f32 v[64:65], v[64:65], v[84:85] op_sel_hi:[1,0]
	global_store_dwordx2 v[20:21], v[18:19], off
	v_pk_mul_f32 v[64:65], v[4:5], v[64:65]
	v_pk_fma_f32 v[24:25], v[24:25], v[64:65], v[68:69]
	v_cvt_pk_bf16_f32 v18, v22, v23
	v_pk_mul_f32 v[80:81], v[80:81], v[84:85] op_sel_hi:[1,0]
	v_pk_mul_f32 v[80:81], v[6:7], v[80:81]
	v_pk_fma_f32 v[26:27], v[26:27], v[80:81], v[50:51]
	v_cvt_pk_bf16_f32 v19, v24, v25
	v_pk_mul_f32 v[58:59], v[58:59], v[84:85] op_sel_hi:[1,0]
	global_store_dwordx2 v[20:21], v[18:19], off offset:512
	v_pk_mul_f32 v[58:59], v[8:9], v[58:59]
	v_pk_fma_f32 v[28:29], v[28:29], v[58:59], v[52:53]
	v_cvt_pk_bf16_f32 v18, v26, v27
	v_cvt_pk_bf16_f32 v19, v28, v29
	v_pk_mul_f32 v[82:83], v[82:83], v[84:85] op_sel_hi:[1,0]
	global_store_dwordx2 v[20:21], v[18:19], off offset:1024
	v_pk_mul_f32 v[82:83], v[16:17], v[82:83]
	v_pk_fma_f32 v[44:45], v[44:45], v[82:83], v[56:57]
	v_cvt_pk_bf16_f32 v18, v42, v43
	v_cvt_pk_bf16_f32 v19, v44, v45
	v_lshl_add_u64 v[40:41], v[40:41], 0, s[16:17]
	global_store_dwordx2 v[20:21], v[18:19], off offset:1536
	s_cbranch_scc0 .LBB0_1716

.LBB0_2016:
	v_pk_mul_f32 v[62:63], v[28:29], v[28:29]
	v_pk_mul_f32 v[64:65], v[26:27], v[26:27]
	v_pk_mul_f32 v[58:59], v[30:31], v[30:31]
	v_pk_mul_f32 v[60:61], v[32:33], v[32:33]
	v_pk_mov_b32 v[66:67], v[64:65], v[62:63] op_sel:[1,0]
	v_mov_b32_e32 v65, v63
	v_pk_add_f32 v[62:63], v[66:67], v[64:65]
	v_pk_mov_b32 v[64:65], v[60:61], v[58:59] op_sel:[1,0]
	v_mov_b32_e32 v61, v59
	v_pk_add_f32 v[58:59], v[64:65], v[60:61]
	s_add_i32 s10, s6, 0xfffffc00
	v_pk_add_f32 v[58:59], v[58:59], v[58:59] op_sel_hi:[0,1]
	v_mul_f32_e32 v58, v40, v40
	s_lshr_b32 s10, s10, 12
	v_pk_fma_f32 v[60:61], v[40:41], v[40:41], v[58:59] op_sel_hi:[1,1,0]
	v_mul_f32_e32 v58, v36, v36
	s_mulk_i32 s10, 0x1800
	s_and_b64 s[4:5], s[4:5], exec
	v_pk_add_f32 v[62:63], v[62:63], v[62:63] op_sel_hi:[0,1]
	v_pk_fma_f32 v[64:65], v[36:37], v[36:37], v[58:59] op_sel_hi:[1,1,0]
	s_cselect_b32 s10, 0x6000, s10
	v_mul_f32_e32 v60, v34, v34
	v_mul_f32_e32 v64, v35, v35
	v_mul_f32_e32 v62, v38, v38
	v_mul_f32_e32 v58, v39, v39
	s_lshl_b64 s[4:5], s[10:11], 2
	v_pk_add_f32 v[66:67], v[60:61], v[64:65]
	v_pk_add_f32 v[68:69], v[62:63], v[58:59]
	v_lshl_add_u64 v[54:55], v[20:21], 0, s[4:5]
	v_lshl_add_u64 v[70:71], v[18:19], 0, s[4:5]
	v_pk_add_f32 v[66:67], v[66:67], v[68:69]
	global_load_dwordx4 v[42:45], v[54:55], off
	global_load_dwordx4 v[46:49], v[54:55], off offset:1024
	global_load_dwordx4 v[50:53], v[54:55], off offset:2048
	s_nop 0
	global_load_dwordx4 v[54:57], v[54:55], off offset:3072
	s_nop 0
	global_load_dwordx4 v[58:61], v[70:71], off offset:2048
	global_load_dwordx4 v[62:65], v[70:71], off offset:3072
	v_add_f32_e32 v74, v66, v67
	global_load_dwordx4 v[66:69], v[70:71], off
	s_nop 0
	global_load_dwordx4 v[70:73], v[70:71], off offset:1024
	v_add_f32_dpp v74, v74, v74 row_ror:8 row_mask:0xf bank_mask:0xf bound_ctrl:1
	s_add_i32 s6, s6, s8
	s_cmpk_lt_i32 s6, 0x4400
	v_add_f32_dpp v74, v74, v74 row_ror:4 row_mask:0xf bank_mask:0xf bound_ctrl:1
	s_waitcnt vmcnt(7)
	v_pk_add_f32 v[42:43], v[42:43], 1.0 op_sel_hi:[1,0]
	v_add_f32_dpp v74, v74, v74 row_ror:2 row_mask:0xf bank_mask:0xf bound_ctrl:1
	v_pk_add_f32 v[44:45], v[44:45], 1.0 op_sel_hi:[1,0]
	s_waitcnt vmcnt(6)
	v_pk_add_f32 v[46:47], v[46:47], 1.0 op_sel_hi:[1,0]
	v_add_f32_dpp v74, v74, v74 row_ror:1 row_mask:0xf bank_mask:0xf bound_ctrl:1
	v_mov_b32_e32 v75, v74
	s_nop 1
	v_permlane16_swap_b32_e32 v74, v75
	v_pk_add_f32 v[48:49], v[48:49], 1.0 op_sel_hi:[1,0]
	s_waitcnt vmcnt(5)
	v_pk_add_f32 v[50:51], v[50:51], 1.0 op_sel_hi:[1,0]
	v_pk_add_f32 v[52:53], v[52:53], 1.0 op_sel_hi:[1,0]
	s_waitcnt vmcnt(4)
	v_pk_add_f32 v[54:55], v[54:55], 1.0 op_sel_hi:[1,0]
	s_waitcnt lgkmcnt(0)
	v_add_f32_e32 v74, v74, v75
	v_mov_b32_e32 v75, v74
	s_nop 1
	v_permlane32_swap_b32_e32 v74, v75
	v_pk_add_f32 v[56:57], v[56:57], 1.0 op_sel_hi:[1,0]
	s_waitcnt lgkmcnt(0)
	v_add_f32_e32 v74, v74, v75
	v_fmamk_f32 v74, v74, 0x3a800000, v89
	v_mul_f32_e32 v75, 0x4f800000, v74
	v_cmp_gt_f32_e32 vcc, s42, v74
	s_nop 1
	v_cndmask_b32_e32 v74, v74, v75, vcc
	v_sqrt_f32_e32 v75, v74
	s_nop 0
	v_add_u32_e32 v76, -1, v75
	v_add_u32_e32 v77, 1, v75
	v_fma_f32 v78, -v76, v75, v74
	v_fma_f32 v79, -v77, v75, v74
	v_cmp_ge_f32_e64 s[4:5], 0, v78
	s_nop 1
	v_cndmask_b32_e64 v75, v75, v76, s[4:5]
	v_cmp_lt_f32_e64 s[4:5], 0, v79
	s_nop 1
	v_cndmask_b32_e64 v75, v75, v77, s[4:5]
	v_mul_f32_e32 v76, 0x37800000, v75
	v_cndmask_b32_e32 v75, v75, v76, vcc
	v_cmp_class_f32_e32 vcc, v74, v90
	s_nop 1
	v_cndmask_b32_e32 v74, v75, v74, vcc
	v_div_scale_f32 v75, s[4:5], v74, v74, 1.0
	v_rcp_f32_e32 v76, v75
	v_div_scale_f32 v77, vcc, 1.0, v74, 1.0
	v_fma_f32 v78, -v75, v76, 1.0
	v_fmac_f32_e32 v76, v78, v76
	v_mul_f32_e32 v78, v77, v76
	v_fma_f32 v79, -v75, v78, v77
	v_fmac_f32_e32 v78, v79, v76
	v_fma_f32 v75, -v75, v78, v77
	v_div_fmas_f32 v75, v75, v76, v78
	v_div_fixup_f32 v74, v75, v74, 1.0
	v_pk_mul_f32 v[26:27], v[26:27], v[74:75] op_sel_hi:[1,0]
	v_pk_mul_f32 v[28:29], v[28:29], v[74:75] op_sel_hi:[1,0]
	v_pk_mul_f32 v[26:27], v[10:11], v[26:27]
	v_pk_mul_f32 v[28:29], v[12:13], v[28:29]
	s_waitcnt vmcnt(1)
	v_pk_fma_f32 v[26:27], v[42:43], v[26:27], v[66:67]
	v_pk_fma_f32 v[28:29], v[44:45], v[28:29], v[68:69]
	v_bfe_u32 v42, v26, 16, 1
	v_add3_u32 v26, v26, v42, s41
	v_bfe_u32 v42, v27, 16, 1
	v_lshrrev_b32_e32 v26, 16, v26
	v_add3_u32 v27, v27, v42, s41
	v_and_or_b32 v26, v27, s3, v26
	v_bfe_u32 v27, v28, 16, 1
	v_add3_u32 v27, v28, v27, s41
	v_bfe_u32 v28, v29, 16, 1
	v_pk_mul_f32 v[32:33], v[32:33], v[74:75] op_sel_hi:[1,0]
	v_lshrrev_b32_e32 v27, 16, v27
	v_add3_u32 v28, v29, v28, s41
	v_pk_mul_f32 v[32:33], v[2:3], v[32:33]
	v_and_or_b32 v27, v28, s3, v27
	v_add_co_u32_e32 v28, vcc, s43, v24
	s_waitcnt vmcnt(0)
	v_pk_fma_f32 v[32:33], v[46:47], v[32:33], v[70:71]
	v_addc_co_u32_e32 v29, vcc, -1, v25, vcc
	v_pk_mul_f32 v[30:31], v[30:31], v[74:75] op_sel_hi:[1,0]
	global_store_dwordx2 v[28:29], v[26:27], off offset:-1536
	v_pk_mul_f32 v[30:31], v[4:5], v[30:31]
	v_pk_fma_f32 v[30:31], v[48:49], v[30:31], v[72:73]
	v_cvt_pk_bf16_f32 v26, v32, v33
	v_bfe_u32 v27, v30, 16, 1
	v_pk_mul_f32 v[40:41], v[40:41], v[74:75] op_sel_hi:[1,0]
	v_add3_u32 v27, v30, v27, s41
	v_bfe_u32 v30, v31, 16, 1
	v_pk_mul_f32 v[40:41], v[6:7], v[40:41]
	v_lshrrev_b32_e32 v27, 16, v27
	v_add3_u32 v30, v31, v30, s41
	v_pk_fma_f32 v[40:41], v[50:51], v[40:41], v[58:59]
	v_and_or_b32 v27, v30, s3, v27
	v_pk_mul_f32 v[36:37], v[36:37], v[74:75] op_sel_hi:[1,0]
	global_store_dwordx2 v[28:29], v[26:27], off offset:-1024
	v_pk_mul_f32 v[36:37], v[8:9], v[36:37]
	v_pk_fma_f32 v[36:37], v[52:53], v[36:37], v[60:61]
	v_cvt_pk_bf16_f32 v26, v40, v41
	v_pk_mul_f32 v[34:35], v[34:35], v[74:75] op_sel_hi:[1,0]
	v_pk_mul_f32 v[34:35], v[14:15], v[34:35]
	v_pk_fma_f32 v[34:35], v[54:55], v[34:35], v[62:63]
	v_cvt_pk_bf16_f32 v27, v36, v37
	v_pk_mul_f32 v[38:39], v[38:39], v[74:75] op_sel_hi:[1,0]
	global_store_dwordx2 v[28:29], v[26:27], off offset:-512
	v_pk_mul_f32 v[38:39], v[16:17], v[38:39]
	v_pk_fma_f32 v[38:39], v[56:57], v[38:39], v[64:65]
	v_cvt_pk_bf16_f32 v26, v34, v35
	v_cvt_pk_bf16_f32 v27, v38, v39
	v_lshl_add_u64 v[24:25], v[24:25], 0, s[12:13]
	global_store_dwordx2 v[28:29], v[26:27], off
	s_cbranch_scc0 .LBB0_2019

.LBB0_2231:
	v_pk_mul_f32 v[62:63], v[32:33], v[32:33]
	v_pk_mul_f32 v[64:65], v[30:31], v[30:31]
	v_pk_mul_f32 v[58:59], v[34:35], v[34:35]
	v_pk_mul_f32 v[60:61], v[38:39], v[38:39]
	v_pk_mov_b32 v[66:67], v[64:65], v[62:63] op_sel:[1,0]
	v_mov_b32_e32 v65, v63
	v_pk_add_f32 v[62:63], v[66:67], v[64:65]
	v_pk_mov_b32 v[64:65], v[60:61], v[58:59] op_sel:[1,0]
	v_mov_b32_e32 v61, v59
	v_pk_add_f32 v[58:59], v[64:65], v[60:61]
	s_add_i32 s10, s6, 0xfffffc00
	v_pk_add_f32 v[58:59], v[58:59], v[58:59] op_sel_hi:[0,1]
	v_mul_f32_e32 v58, v44, v44
	s_lshr_b32 s10, s10, 12
	v_pk_fma_f32 v[60:61], v[44:45], v[44:45], v[58:59] op_sel_hi:[1,1,0]
	v_mul_f32_e32 v58, v40, v40
	s_mulk_i32 s10, 0x1800
	s_and_b64 s[4:5], s[4:5], exec
	v_pk_add_f32 v[62:63], v[62:63], v[62:63] op_sel_hi:[0,1]
	v_pk_fma_f32 v[64:65], v[40:41], v[40:41], v[58:59] op_sel_hi:[1,1,0]
	s_cselect_b32 s10, 0x6000, s10
	v_mul_f32_e32 v60, v36, v36
	v_mul_f32_e32 v64, v37, v37
	v_mul_f32_e32 v62, v42, v42
	v_mul_f32_e32 v58, v43, v43
	s_lshl_b64 s[4:5], s[10:11], 2
	v_pk_add_f32 v[66:67], v[60:61], v[64:65]
	v_pk_add_f32 v[68:69], v[62:63], v[58:59]
	v_lshl_add_u64 v[54:55], v[24:25], 0, s[4:5]
	v_lshl_add_u64 v[70:71], v[22:23], 0, s[4:5]
	v_pk_add_f32 v[66:67], v[66:67], v[68:69]
	global_load_dwordx4 v[18:21], v[54:55], off
	global_load_dwordx4 v[46:49], v[54:55], off offset:1024
	global_load_dwordx4 v[50:53], v[54:55], off offset:2048
	s_nop 0
	global_load_dwordx4 v[54:57], v[54:55], off offset:3072
	s_nop 0
	global_load_dwordx4 v[58:61], v[70:71], off offset:2048
	global_load_dwordx4 v[62:65], v[70:71], off offset:3072
	v_add_f32_e32 v74, v66, v67
	global_load_dwordx4 v[66:69], v[70:71], off
	s_nop 0
	global_load_dwordx4 v[70:73], v[70:71], off offset:1024
	v_add_f32_dpp v74, v74, v74 row_ror:8 row_mask:0xf bank_mask:0xf bound_ctrl:1
	s_add_i32 s6, s6, s8
	s_cmpk_lt_i32 s6, 0x4400
	v_add_f32_dpp v74, v74, v74 row_ror:4 row_mask:0xf bank_mask:0xf bound_ctrl:1
	s_waitcnt vmcnt(7)
	v_pk_add_f32 v[18:19], v[18:19], 1.0 op_sel_hi:[1,0]
	v_add_f32_dpp v74, v74, v74 row_ror:2 row_mask:0xf bank_mask:0xf bound_ctrl:1
	v_pk_add_f32 v[20:21], v[20:21], 1.0 op_sel_hi:[1,0]
	s_waitcnt vmcnt(6)
	v_pk_add_f32 v[46:47], v[46:47], 1.0 op_sel_hi:[1,0]
	v_add_f32_dpp v74, v74, v74 row_ror:1 row_mask:0xf bank_mask:0xf bound_ctrl:1
	v_mov_b32_e32 v75, v74
	s_nop 1
	v_permlane16_swap_b32_e32 v74, v75
	v_pk_add_f32 v[48:49], v[48:49], 1.0 op_sel_hi:[1,0]
	s_waitcnt vmcnt(5)
	v_pk_add_f32 v[50:51], v[50:51], 1.0 op_sel_hi:[1,0]
	v_pk_add_f32 v[52:53], v[52:53], 1.0 op_sel_hi:[1,0]
	s_waitcnt vmcnt(4)
	v_pk_add_f32 v[54:55], v[54:55], 1.0 op_sel_hi:[1,0]
	s_waitcnt lgkmcnt(0)
	v_add_f32_e32 v74, v74, v75
	v_mov_b32_e32 v75, v74
	s_nop 1
	v_permlane32_swap_b32_e32 v74, v75
	v_pk_add_f32 v[56:57], v[56:57], 1.0 op_sel_hi:[1,0]
	s_waitcnt lgkmcnt(0)
	v_add_f32_e32 v74, v74, v75
	v_fmamk_f32 v74, v74, 0x3a800000, v95
	v_mul_f32_e32 v75, 0x4f800000, v74
	v_cmp_gt_f32_e32 vcc, s41, v74
	s_nop 1
	v_cndmask_b32_e32 v74, v74, v75, vcc
	v_sqrt_f32_e32 v75, v74
	s_nop 0
	v_add_u32_e32 v76, -1, v75
	v_add_u32_e32 v77, 1, v75
	v_fma_f32 v78, -v76, v75, v74
	v_fma_f32 v79, -v77, v75, v74
	v_cmp_ge_f32_e64 s[4:5], 0, v78
	s_nop 1
	v_cndmask_b32_e64 v75, v75, v76, s[4:5]
	v_cmp_lt_f32_e64 s[4:5], 0, v79
	s_nop 1
	v_cndmask_b32_e64 v75, v75, v77, s[4:5]
	v_mul_f32_e32 v76, 0x37800000, v75
	v_cndmask_b32_e32 v75, v75, v76, vcc
	v_cmp_class_f32_e32 vcc, v74, v96
	s_nop 1
	v_cndmask_b32_e32 v74, v75, v74, vcc
	v_div_scale_f32 v75, s[4:5], v74, v74, 1.0
	v_rcp_f32_e32 v76, v75
	v_div_scale_f32 v77, vcc, 1.0, v74, 1.0
	v_fma_f32 v78, -v75, v76, 1.0
	v_fmac_f32_e32 v76, v78, v76
	v_mul_f32_e32 v78, v77, v76
	v_fma_f32 v79, -v75, v78, v77
	v_fmac_f32_e32 v78, v79, v76
	v_fma_f32 v75, -v75, v78, v77
	v_div_fmas_f32 v75, v75, v76, v78
	v_div_fixup_f32 v74, v75, v74, 1.0
	v_pk_mul_f32 v[30:31], v[30:31], v[74:75] op_sel_hi:[1,0]
	v_pk_mul_f32 v[32:33], v[32:33], v[74:75] op_sel_hi:[1,0]
	v_pk_mul_f32 v[30:31], v[10:11], v[30:31]
	v_pk_mul_f32 v[32:33], v[12:13], v[32:33]
	s_waitcnt vmcnt(1)
	v_pk_fma_f32 v[18:19], v[18:19], v[30:31], v[66:67]
	v_pk_fma_f32 v[20:21], v[20:21], v[32:33], v[68:69]
	v_bfe_u32 v30, v18, 16, 1
	v_add3_u32 v18, v18, v30, s40
	v_bfe_u32 v30, v19, 16, 1
	v_lshrrev_b32_e32 v18, 16, v18
	v_add3_u32 v19, v19, v30, s40
	v_and_or_b32 v18, v19, s3, v18
	v_bfe_u32 v19, v20, 16, 1
	v_add3_u32 v19, v20, v19, s40
	v_bfe_u32 v20, v21, 16, 1
	v_pk_mul_f32 v[38:39], v[38:39], v[74:75] op_sel_hi:[1,0]
	v_lshrrev_b32_e32 v19, 16, v19
	v_add3_u32 v20, v21, v20, s40
	v_pk_mul_f32 v[38:39], v[2:3], v[38:39]
	v_and_or_b32 v19, v20, s3, v19
	v_add_co_u32_e32 v20, vcc, s42, v28
	s_waitcnt vmcnt(0)
	v_pk_fma_f32 v[38:39], v[46:47], v[38:39], v[70:71]
	v_addc_co_u32_e32 v21, vcc, -1, v29, vcc
	v_pk_mul_f32 v[34:35], v[34:35], v[74:75] op_sel_hi:[1,0]
	global_store_dwordx2 v[20:21], v[18:19], off offset:-1536
	v_pk_mul_f32 v[34:35], v[4:5], v[34:35]
	v_pk_fma_f32 v[34:35], v[48:49], v[34:35], v[72:73]
	v_cvt_pk_bf16_f32 v18, v38, v39
	v_pk_mul_f32 v[44:45], v[44:45], v[74:75] op_sel_hi:[1,0]
	v_pk_mul_f32 v[44:45], v[6:7], v[44:45]
	v_pk_fma_f32 v[44:45], v[50:51], v[44:45], v[58:59]
	v_cvt_pk_bf16_f32 v19, v34, v35
	v_pk_mul_f32 v[40:41], v[40:41], v[74:75] op_sel_hi:[1,0]
	global_store_dwordx2 v[20:21], v[18:19], off offset:-1024
	v_pk_mul_f32 v[40:41], v[8:9], v[40:41]
	v_pk_fma_f32 v[40:41], v[52:53], v[40:41], v[60:61]
	v_cvt_pk_bf16_f32 v18, v44, v45
	v_pk_mul_f32 v[36:37], v[36:37], v[74:75] op_sel_hi:[1,0]
	v_pk_mul_f32 v[36:37], v[14:15], v[36:37]
	v_pk_fma_f32 v[36:37], v[54:55], v[36:37], v[62:63]
	v_cvt_pk_bf16_f32 v19, v40, v41
	v_pk_mul_f32 v[42:43], v[42:43], v[74:75] op_sel_hi:[1,0]
	global_store_dwordx2 v[20:21], v[18:19], off offset:-512
	v_pk_mul_f32 v[42:43], v[16:17], v[42:43]
	v_pk_fma_f32 v[42:43], v[56:57], v[42:43], v[64:65]
	v_cvt_pk_bf16_f32 v18, v36, v37
	v_cvt_pk_bf16_f32 v19, v42, v43
	v_lshl_add_u64 v[28:29], v[28:29], 0, s[12:13]
	global_store_dwordx2 v[20:21], v[18:19], off
	s_cbranch_scc0 .LBB0_2234

.LBB0_3066:
	s_waitcnt vmcnt(5)
	v_pk_mul_f32 v[54:55], v[80:81], v[54:55] op_sel_hi:[0,1]
	v_pk_mul_f32 v[52:53], v[80:81], v[52:53] op_sel_hi:[0,1]
	v_lshlrev_b32_e32 v88, 16, v86
	v_and_b32_e32 v89, 0xffff0000, v86
	v_lshlrev_b32_e32 v86, 16, v87
	v_and_b32_e32 v87, 0xffff0000, v87
	s_waitcnt vmcnt(4)
	v_pk_fma_f32 v[44:45], v[82:83], v[44:45], v[52:53] op_sel_hi:[0,1,1]
	v_pk_fma_f32 v[46:47], v[82:83], v[46:47], v[54:55] op_sel_hi:[0,1,1]
	v_pk_mul_f32 v[38:39], v[80:81], v[38:39] op_sel_hi:[0,1]
	v_pk_mul_f32 v[36:37], v[80:81], v[36:37] op_sel_hi:[0,1]
	s_waitcnt vmcnt(1)
	v_pk_fma_f32 v[42:43], v[42:43], v[46:47], v[86:87]
	v_pk_fma_f32 v[40:41], v[40:41], v[44:45], v[88:89]
	v_lshlrev_b32_e32 v44, 16, v84
	v_and_b32_e32 v45, 0xffff0000, v84
	v_lshlrev_b32_e32 v46, 16, v85
	v_and_b32_e32 v47, 0xffff0000, v85
	v_pk_fma_f32 v[34:35], v[82:83], v[34:35], v[38:39] op_sel_hi:[0,1,1]
	v_pk_fma_f32 v[32:33], v[82:83], v[32:33], v[36:37] op_sel_hi:[0,1,1]
	v_pk_mul_f32 v[26:27], v[80:81], v[26:27] op_sel_hi:[0,1]
	v_pk_mul_f32 v[24:25], v[80:81], v[24:25] op_sel_hi:[0,1]
	v_pk_fma_f32 v[28:29], v[28:29], v[32:33], v[44:45]
	v_pk_fma_f32 v[30:31], v[30:31], v[34:35], v[46:47]
	v_lshlrev_b32_e32 v32, 16, v78
	v_and_b32_e32 v33, 0xffff0000, v78
	v_lshlrev_b32_e32 v34, 16, v79
	v_and_b32_e32 v35, 0xffff0000, v79
	v_pk_fma_f32 v[22:23], v[82:83], v[22:23], v[26:27] op_sel_hi:[0,1,1]
	v_pk_fma_f32 v[20:21], v[82:83], v[20:21], v[24:25] op_sel_hi:[0,1,1]
	v_pk_mul_f32 v[24:25], v[80:81], v[62:63] op_sel_hi:[0,1]
	v_pk_mul_f32 v[26:27], v[80:81], v[60:61] op_sel_hi:[0,1]
	v_pk_fma_f32 v[16:17], v[16:17], v[20:21], v[32:33]
	v_pk_fma_f32 v[18:19], v[18:19], v[22:23], v[34:35]
	v_lshlrev_b32_e32 v20, 16, v76
	v_and_b32_e32 v21, 0xffff0000, v76
	v_lshlrev_b32_e32 v22, 16, v77
	v_and_b32_e32 v23, 0xffff0000, v77
	v_pk_fma_f32 v[26:27], v[82:83], v[56:57], v[26:27] op_sel_hi:[0,1,1]
	v_pk_fma_f32 v[24:25], v[82:83], v[58:59], v[24:25] op_sel_hi:[0,1,1]
	s_waitcnt vmcnt(0)
	v_pk_fma_f32 v[22:23], v[50:51], v[24:25], v[22:23]
	v_pk_fma_f32 v[20:21], v[48:49], v[26:27], v[20:21]
	v_pk_mul_f32 v[24:25], v[18:19], v[18:19]
	v_pk_mul_f32 v[26:27], v[16:17], v[16:17]
	v_mov_b32_e32 v33, v25
	v_mov_b32_e32 v32, v26
	v_pk_mov_b32 v[24:25], v[26:27], v[24:25] op_sel:[1,0]
	v_pk_mul_f32 v[26:27], v[30:31], v[30:31]
	v_pk_add_f32 v[24:25], v[24:25], v[32:33]
	v_pk_mul_f32 v[32:33], v[28:29], v[28:29]
	v_mov_b32_e32 v35, v27
	v_mov_b32_e32 v34, v32
	v_pk_mov_b32 v[26:27], v[32:33], v[26:27] op_sel:[1,0]
	v_mul_f32_e32 v32, v20, v20
	v_pk_add_f32 v[26:27], v[26:27], v[34:35]
	v_mul_f32_e32 v33, v21, v21
	v_pk_add_f32 v[24:25], v[24:25], v[24:25] op_sel:[0,1] op_sel_hi:[1,0]
	v_pk_add_f32 v[26:27], v[26:27], v[26:27] op_sel:[0,1] op_sel_hi:[1,0]
	v_mov_b32_e32 v25, v32
	v_mov_b32_e32 v27, v33
	v_pk_add_f32 v[24:25], v[24:25], v[26:27]
	v_mul_f32_e32 v26, v41, v41
	v_mul_f32_e32 v32, v43, v43
	v_mul_f32_e32 v34, v22, v22
	v_mul_f32_e32 v35, v23, v23
	v_pk_fma_f32 v[26:27], v[40:41], v[40:41], v[26:27] op_sel_hi:[1,1,0]
	v_pk_fma_f32 v[32:33], v[42:43], v[42:43], v[32:33] op_sel_hi:[1,1,0]
	v_mov_b32_e32 v27, v34
	v_mov_b32_e32 v33, v35
	v_pk_add_f32 v[26:27], v[26:27], v[32:33]
	s_ashr_i32 s5, s4, 31
	v_pk_add_f32 v[24:25], v[24:25], v[26:27]
	s_add_i32 s10, s10, s16
	v_add_f32_e32 v24, v24, v25
	v_lshl_add_u64 v[72:73], v[72:73], 0, s[12:13]
	s_nop 0
	v_add_f32_dpp v24, v24, v24 row_ror:8 row_mask:0xf bank_mask:0xf bound_ctrl:1
	s_nop 1
	v_add_f32_dpp v24, v24, v24 row_ror:4 row_mask:0xf bank_mask:0xf bound_ctrl:1
	s_nop 1
	v_add_f32_dpp v24, v24, v24 row_ror:2 row_mask:0xf bank_mask:0xf bound_ctrl:1
	s_nop 1
	v_add_f32_dpp v24, v24, v24 row_ror:1 row_mask:0xf bank_mask:0xf bound_ctrl:1
	v_mov_b32_e32 v25, v24
	s_nop 1
	v_permlane16_swap_b32_e32 v24, v25
	s_waitcnt lgkmcnt(0)
	v_add_f32_e32 v24, v24, v25
	v_mov_b32_e32 v25, v24
	s_nop 1
	v_permlane32_swap_b32_e32 v24, v25
	s_waitcnt lgkmcnt(0)
	v_add_f32_e32 v24, v24, v25
	v_fmamk_f32 v24, v24, 0x3a800000, v92
	v_mul_f32_e32 v25, 0x4f800000, v24
	v_cmp_gt_f32_e32 vcc, s19, v24
	s_nop 1
	v_cndmask_b32_e32 v24, v24, v25, vcc
	v_sqrt_f32_e32 v25, v24
	s_nop 0
	v_add_u32_e32 v26, -1, v25
	v_fma_f32 v27, -v26, v25, v24
	v_cmp_ge_f32_e64 s[0:1], 0, v27
	v_add_u32_e32 v27, 1, v25
	s_nop 0
	v_cndmask_b32_e64 v26, v25, v26, s[0:1]
	v_fma_f32 v25, -v27, v25, v24
	v_cmp_lt_f32_e64 s[0:1], 0, v25
	s_nop 1
	v_cndmask_b32_e64 v25, v26, v27, s[0:1]
	v_mul_f32_e32 v26, 0x37800000, v25
	v_cndmask_b32_e32 v25, v25, v26, vcc
	v_cmp_class_f32_e32 vcc, v24, v93
	s_nop 1
	v_cndmask_b32_e32 v24, v25, v24, vcc
	v_div_scale_f32 v25, s[0:1], v24, v24, 1.0
	v_rcp_f32_e32 v26, v25
	s_lshl_b64 s[0:1], s[4:5], 12
	s_add_i32 s4, s4, s6
	v_fma_f32 v27, -v25, v26, 1.0
	v_fmac_f32_e32 v26, v27, v26
	v_div_scale_f32 v27, vcc, 1.0, v24, 1.0
	v_mul_f32_e32 v32, v27, v26
	v_fma_f32 v33, -v25, v32, v27
	v_fmac_f32_e32 v32, v33, v26
	v_fma_f32 v25, -v25, v32, v27
	v_div_fmas_f32 v25, v25, v26, v32
	v_div_fixup_f32 v24, v25, v24, 1.0
	v_pk_mul_f32 v[16:17], v[16:17], v[24:25] op_sel_hi:[1,0]
	v_pk_mul_f32 v[18:19], v[18:19], v[24:25] op_sel_hi:[1,0]
	v_lshl_add_u64 v[26:27], v[70:71], 0, s[0:1]
	v_pk_mul_f32 v[18:19], v[2:3], v[18:19]
	v_pk_mul_f32 v[16:17], v[0:1], v[16:17]
	global_store_dwordx4 v[26:27], v[16:19], off
	s_add_i32 s0, s4, 0x400
	s_cmpk_lt_i32 s0, 0x4400
	v_pk_mul_f32 v[16:17], v[28:29], v[24:25] op_sel_hi:[1,0]
	v_pk_mul_f32 v[18:19], v[30:31], v[24:25] op_sel_hi:[1,0]
	v_pk_mul_f32 v[16:17], v[4:5], v[16:17]
	v_pk_mul_f32 v[18:19], v[6:7], v[18:19]
	global_store_dwordx4 v[26:27], v[16:19], off offset:1024
	s_nop 1
	v_pk_mul_f32 v[16:17], v[40:41], v[24:25] op_sel_hi:[1,0]
	v_pk_mul_f32 v[18:19], v[42:43], v[24:25] op_sel_hi:[1,0]
	v_pk_mul_f32 v[16:17], v[8:9], v[16:17]
	v_pk_mul_f32 v[18:19], v[10:11], v[18:19]
	global_store_dwordx4 v[26:27], v[16:19], off offset:2048
	s_nop 1
	v_pk_mul_f32 v[16:17], v[20:21], v[24:25] op_sel_hi:[1,0]
	v_pk_mul_f32 v[18:19], v[22:23], v[24:25] op_sel_hi:[1,0]
	v_pk_mul_f32 v[16:17], v[12:13], v[16:17]
	v_pk_mul_f32 v[18:19], v[14:15], v[18:19]
	global_store_dwordx4 v[26:27], v[16:19], off offset:3072
	s_cbranch_scc0 .LBB0_3099
